# GEMM phase prologues (12 sites): K-tile 1's six LDS-DMA loads issued before the first wait+barrier, wait becomes vmcnt(8)
# speedup vs baseline: 1.0104x; 1.0104x over previous
.LBB0_1015:
	s_add_u32 s8, s28, 0x38000000
	s_addc_u32 s9, s29, 0
	s_add_i32 s78, s68, 0x18000
	s_mov_b32 m0, s78
	s_movk_i32 s1, 0x80
	s_add_i32 s79, s68, 0x1a000
	buffer_load_dwordx4 v245, s[52:55], s1 offen lds
	s_mov_b32 m0, s79
	s_add_i32 s80, s68, 0x8000
	buffer_load_dwordx4 v244, s[52:55], s1 offen lds
	s_mov_b32 s42, s54
	s_mov_b32 s43, s55
	s_mov_b32 m0, s80
	s_add_i32 s82, s68, 0xa000
	buffer_load_dwordx4 v132, s[40:43], s1 offen lds
	s_mov_b32 m0, s82
	s_add_i32 s83, s68, 0x1c000
	buffer_load_dwordx4 v133, s[40:43], s1 offen lds
	s_mov_b32 m0, s83
	s_mov_b32 s1, 0x40080
	s_add_i32 s88, s68, 0x1e000
	buffer_load_dwordx4 v245, s[52:55], s1 offen lds
	s_mov_b32 m0, s88
	s_sext_i32_i16 s95, s4
	buffer_load_dwordx4 v244, s[52:55], s1 offen lds
	s_waitcnt vmcnt(8)
	s_barrier
	v_and_b32_e32 v1, 48, v0
	v_lshlrev_b32_e32 v2, 6, v0
	s_movk_i32 s4, 0x3c0
	v_lshlrev_b32_e32 v0, 2, v0
	s_lshl_b32 s1, s12, 13
	v_and_or_b32 v1, v2, s4, v1
	v_and_b32_e32 v0, 32, v0
	v_bitop3_b32 v2, v1, s1, v0 bitop3:0xde
	s_lshl_b32 s1, s5, 5
	s_and_b32 s90, s1, 0x60
	s_lshl_b32 s1, s90, 7
	s_lshl_b32 s89, s12, 6
	v_bitop3_b32 v0, v1, s1, v0 bitop3:0xde
	s_waitcnt vmcnt(6)
	s_add_i32 s91, s68, 0xc000
	s_cmp_lt_u32 s5, 4
	v_add_u32_e32 v0, 0, v0
	v_mov_b32_e32 v13, v12
	v_mov_b32_e32 v14, v12
	v_mov_b32_e32 v15, v12
	s_cselect_b64 s[18:19], -1, 0
	s_add_i32 s92, s68, 0xe000
	s_ashr_i32 s93, s56, 31
	s_mov_b32 s94, 0
	s_mov_b64 s[64:65], -1
	v_add_u32_e32 v134, 0x10000, v0
	v_add_u32_e32 v135, 0x14000, v0
	v_add_u32_e32 v136, 0, v2
	v_add_u32_e32 v137, 0x18000, v0
	v_add_u32_e32 v138, 0x1c000, v0
	s_mov_b64 s[42:43], s[54:55]
	s_mov_b64 s[4:5], s[54:55]
	s_barrier
	s_branch .LBB0_1018

.LBB0_1041:
	s_lshl_b32 s80, s51, 7
	s_lshl_b64 s[18:19], s[80:81], 2
	s_waitcnt lgkmcnt(0)
	s_add_u32 s72, s0, s18
	s_addc_u32 s73, s1, s19
	s_add_u32 s0, s2, s18
	s_addc_u32 s1, s3, s19
	v_writelane_b32 v255, s0, 29
	s_movk_i32 s3, 0x80
	v_writelane_b32 v255, s1, 30
	s_add_u32 s0, s4, s18
	s_addc_u32 s1, s5, s19
	v_writelane_b32 v255, s0, 31
	s_lshl_b32 s78, s8, 6
	s_mov_b32 s42, s54
	v_writelane_b32 v255, s1, 32
	s_and_b32 s0, s12, 3
	s_lshl_b32 s1, s8, 13
	s_lshl_b32 s79, s0, 5
	s_lshl_b32 s2, s0, 12
	s_add_u32 s18, s28, 0x31000000
	s_addc_u32 s19, s29, 0
	s_add_u32 s20, s28, 0x33000000
	s_addc_u32 s21, s29, 0
	s_add_u32 s4, s28, 0x37000000
	s_addc_u32 s5, s29, 0
	s_add_i32 s69, s92, 0x18000
	s_mov_b32 m0, s69
	s_add_i32 s61, s92, 0x1a000
	buffer_load_dwordx4 v146, s[52:55], s3 offen lds
	s_mov_b32 m0, s61
	s_add_i32 s71, s92, 0x8000
	buffer_load_dwordx4 v147, s[52:55], s3 offen lds
	s_mov_b32 s43, s55
	s_mov_b32 m0, s71
	s_add_i32 s70, s92, 0xa000
	buffer_load_dwordx4 v148, s[40:43], s3 offen lds
	s_mov_b32 m0, s70
	s_add_i32 s83, s92, 0x1c000
	buffer_load_dwordx4 v149, s[40:43], s3 offen lds
	s_mov_b32 m0, s83
	s_mov_b32 s3, 0x40080
	s_add_i32 s82, s92, 0x1e000
	buffer_load_dwordx4 v146, s[52:55], s3 offen lds
	s_mov_b32 m0, s82
	v_and_b32_e32 v1, 48, v0
	buffer_load_dwordx4 v147, s[52:55], s3 offen lds
	s_waitcnt vmcnt(8)
	s_barrier
	v_lshlrev_b32_e32 v2, 6, v0
	s_movk_i32 s3, 0x3c0
	v_lshlrev_b32_e32 v0, 2, v0
	s_add_i32 s89, s92, 0xc000
	v_and_or_b32 v1, v2, s3, v1
	v_and_b32_e32 v0, 32, v0
	s_cmp_lt_u32 s12, 4
	v_bitop3_b32 v2, v1, s1, v0 bitop3:0xde
	s_waitcnt vmcnt(6)
	s_cselect_b64 s[62:63], -1, 0
	s_lshl_b32 s1, s0, 2
	v_writelane_b32 v255, s4, 33
	v_bitop3_b32 v0, v1, s2, v0 bitop3:0xde
	s_add_i32 s90, s1, 0
	v_writelane_b32 v255, s5, 34
	v_mov_b32_e32 v17, v16
	v_mov_b32_e32 v18, v16
	v_mov_b32_e32 v19, v16
	s_add_i32 s90, s90, 0x20500
	s_lshl_b32 s91, s0, 7
	s_add_i32 s88, s92, 0xe000
	s_ashr_i32 s93, s56, 31
	s_ashr_i32 s94, s57, 31
	s_mov_b32 s95, 0
	s_mov_b64 s[4:5], -1
	v_add_u32_e32 v150, 0, v0
	v_add_u32_e32 v151, 0, v2
	s_mov_b64 s[42:43], s[54:55]
	s_mov_b64 s[0:1], s[54:55]
	s_barrier
	s_branch .LBB0_1044

.LBB0_1173:
	s_and_b32 s73, s5, 3
	s_lshl_b32 s8, s12, 13
	s_lshl_b32 s9, s73, 12
	s_add_u32 s2, s28, 0x35000000
	s_addc_u32 s3, s29, 0
	s_add_i32 s76, s63, 0x18000
	s_mov_b32 m0, s76
	s_movk_i32 s13, 0x80
	s_add_i32 s77, s63, 0x1a000
	buffer_load_dwordx4 v144, s[52:55], s13 offen lds
	s_mov_b32 m0, s77
	s_add_i32 s78, s63, 0x8000
	buffer_load_dwordx4 v145, s[52:55], s13 offen lds
	s_mov_b32 s42, s54
	s_mov_b32 s43, s55
	s_mov_b32 m0, s78
	s_add_i32 s79, s63, 0xa000
	buffer_load_dwordx4 v146, s[40:43], s13 offen lds
	s_mov_b32 m0, s79
	s_add_i32 s80, s63, 0x1c000
	buffer_load_dwordx4 v147, s[40:43], s13 offen lds
	s_mov_b32 m0, s80
	s_mov_b32 s13, 0x40080
	s_add_i32 s82, s63, 0x1e000
	buffer_load_dwordx4 v144, s[52:55], s13 offen lds
	s_mov_b32 m0, s82
	v_and_b32_e32 v5, 15, v4
	buffer_load_dwordx4 v145, s[52:55], s13 offen lds
	s_waitcnt vmcnt(8)
	s_barrier
	v_and_b32_e32 v6, 48, v4
	v_lshlrev_b32_e32 v4, 2, v4
	s_add_i32 s83, s63, 0xc000
	v_lshl_or_b32 v5, v5, 6, v6
	v_and_b32_e32 v4, 32, v4
	s_cmp_lt_u32 s5, 4
	s_sext_i32_i16 s94, s4
	v_bitop3_b32 v6, v5, s8, v4 bitop3:0xde
	v_bitop3_b32 v4, v5, s9, v4 bitop3:0xde
	s_waitcnt vmcnt(6)
	s_cselect_b64 s[8:9], -1, 0
	s_lshl_b32 s4, s73, 7
	s_add_i32 s88, s4, 0
	v_mov_b32_e32 v1, v0
	v_mov_b32_e32 v2, v0
	v_mov_b32_e32 v3, v0
	s_add_i32 s88, s88, 0x20100
	s_lshl_b32 s89, s12, 8
	s_and_b32 s90, s5, 4
	s_add_i32 s91, s63, 0xe000
	s_ashr_i32 s92, s56, 31
	s_mov_b32 s93, 0
	v_add_u32_e32 v148, 0, v4
	v_add_u32_e32 v149, 0, v6
	s_mov_b64 s[42:43], s[54:55]
	s_mov_b64 s[4:5], s[54:55]
	s_barrier
	s_branch .LBB0_1176

.LBB0_1203:
	s_and_b32 s5, s4, 3
	s_lshl_b32 s72, s2, 6
	s_lshl_b32 s8, s2, 13
	s_lshl_b32 s73, s5, 5
	s_lshl_b32 s9, s5, 12
	s_add_u32 s2, s28, 0x44000000
	s_addc_u32 s3, s29, 0
	s_add_i32 s76, s64, 0x18000
	s_mov_b32 m0, s76
	s_movk_i32 s12, 0x80
	s_add_i32 s77, s64, 0x1a000
	buffer_load_dwordx4 v146, s[52:55], s12 offen lds
	s_mov_b32 m0, s77
	s_add_i32 s78, s64, 0x8000
	buffer_load_dwordx4 v147, s[52:55], s12 offen lds
	s_mov_b32 s42, s54
	s_mov_b32 s43, s55
	s_mov_b32 m0, s78
	s_add_i32 s79, s64, 0xa000
	buffer_load_dwordx4 v148, s[40:43], s12 offen lds
	s_mov_b32 m0, s79
	s_add_i32 s80, s64, 0x1c000
	buffer_load_dwordx4 v149, s[40:43], s12 offen lds
	s_mov_b32 m0, s80
	s_movk_i32 s12, 0x1080
	s_add_i32 s82, s64, 0x1e000
	buffer_load_dwordx4 v146, s[52:55], s12 offen lds
	s_mov_b32 m0, s82
	v_and_b32_e32 v5, 48, v4
	buffer_load_dwordx4 v147, s[52:55], s12 offen lds
	s_waitcnt vmcnt(8)
	s_barrier
	v_lshlrev_b32_e32 v6, 6, v4
	s_movk_i32 s12, 0x3c0
	v_lshlrev_b32_e32 v4, 2, v4
	s_add_i32 s83, s64, 0xc000
	v_and_or_b32 v5, v6, s12, v5
	v_and_b32_e32 v4, 32, v4
	s_cmp_lt_u32 s4, 4
	v_bitop3_b32 v6, v5, s8, v4 bitop3:0xde
	v_bitop3_b32 v4, v5, s9, v4 bitop3:0xde
	s_waitcnt vmcnt(6)
	s_cselect_b64 s[8:9], -1, 0
	s_lshl_b32 s4, s5, 7
	s_add_i32 s88, s4, 0
	v_mov_b32_e32 v1, v0
	v_mov_b32_e32 v2, v0
	v_mov_b32_e32 v3, v0
	s_add_i32 s88, s88, 0x20100
	s_ashr_i32 s89, s72, 31
	s_add_i32 s90, s64, 0xe000
	s_ashr_i32 s91, s56, 31
	s_mov_b32 s92, 0
	v_add_u32_e32 v150, 0, v4
	v_add_u32_e32 v151, 0, v6
	s_mov_b64 s[42:43], s[54:55]
	s_mov_b64 s[4:5], s[54:55]
	s_barrier
	s_branch .LBB0_1206

.LBB0_1381:
	s_add_i32 s31, s13, 0x18000
	s_mov_b32 m0, s31
	s_movk_i32 s4, 0x80
	s_add_i32 s33, s13, 0x1a000
	buffer_load_dwordx4 v160, s[52:55], s4 offen lds
	s_mov_b32 m0, s33
	s_add_i32 s34, s13, 0x8000
	buffer_load_dwordx4 v161, s[52:55], s4 offen lds
	s_mov_b32 s42, s54
	s_mov_b32 s43, s55
	s_mov_b32 m0, s34
	s_add_i32 s35, s13, 0xa000
	buffer_load_dwordx4 v162, s[40:43], s4 offen lds
	s_mov_b32 m0, s35
	s_add_i32 s62, s13, 0x1c000
	buffer_load_dwordx4 v163, s[40:43], s4 offen lds
	s_mov_b32 m0, s62
	s_mov_b32 s4, 0xa0080
	s_add_i32 s63, s13, 0x1e000
	buffer_load_dwordx4 v160, s[52:55], s4 offen lds
	s_mov_b32 m0, s63
	s_sext_i32_i8 s44, s1
	buffer_load_dwordx4 v161, s[52:55], s4 offen lds
	s_waitcnt vmcnt(8)
	s_barrier
	v_and_b32_e32 v5, 48, v4
	v_lshlrev_b32_e32 v6, 6, v4
	s_movk_i32 s1, 0x3c0
	v_lshlrev_b32_e32 v4, 2, v4
	s_lshl_b32 s64, s0, 6
	s_lshl_b32 s0, s0, 13
	v_and_or_b32 v5, v6, s1, v5
	v_and_b32_e32 v4, 32, v4
	v_bitop3_b32 v6, v5, s0, v4 bitop3:0xde
	s_lshl_b32 s0, s3, 5
	s_and_b32 s65, s0, 0x60
	s_lshl_b32 s0, s65, 7
	s_waitcnt vmcnt(6)
	s_ashr_i32 s74, s64, 31
	s_add_i32 s75, s13, 0xc000
	v_bitop3_b32 v4, v5, s0, v4 bitop3:0xde
	s_cmp_lt_u32 s3, 4
	v_mov_b32_e32 v1, v0
	v_mov_b32_e32 v2, v0
	v_mov_b32_e32 v3, v0
	s_cselect_b64 s[68:69], -1, 0
	s_add_i32 s78, s13, 0xe000
	s_ashr_i32 s79, s8, 31
	s_mov_b32 s96, 0
	v_add_u32_e32 v164, 0, v4
	v_add_u32_e32 v165, 0, v6
	s_mov_b64 s[42:43], s[54:55]
	s_mov_b64 s[0:1], s[54:55]
	s_barrier
	s_branch .LBB0_1384

.LBB0_1413:
	s_add_i32 s34, s74, 0x18000
	s_mov_b32 m0, s34
	s_movk_i32 s4, 0x80
	s_add_i32 s35, s74, 0x1a000
	buffer_load_dwordx4 v160, s[52:55], s4 offen lds
	s_mov_b32 m0, s35
	s_add_i32 s62, s74, 0x8000
	buffer_load_dwordx4 v161, s[52:55], s4 offen lds
	s_mov_b32 s42, s54
	s_mov_b32 s43, s55
	s_mov_b32 m0, s62
	s_add_i32 s63, s74, 0xa000
	buffer_load_dwordx4 v162, s[40:43], s4 offen lds
	s_mov_b32 m0, s63
	s_add_i32 s64, s74, 0x1c000
	buffer_load_dwordx4 v163, s[40:43], s4 offen lds
	s_mov_b32 m0, s64
	s_mov_b32 s4, 0xa0080
	s_add_i32 s65, s74, 0x1e000
	buffer_load_dwordx4 v160, s[52:55], s4 offen lds
	s_mov_b32 m0, s65
	s_sext_i32_i8 s44, s1
	buffer_load_dwordx4 v161, s[52:55], s4 offen lds
	s_waitcnt vmcnt(8)
	s_barrier
	v_and_b32_e32 v1, 48, v0
	v_lshlrev_b32_e32 v2, 6, v0
	s_movk_i32 s1, 0x3c0
	v_lshlrev_b32_e32 v0, 2, v0
	s_lshl_b32 s78, s0, 6
	s_lshl_b32 s0, s0, 13
	v_and_or_b32 v1, v2, s1, v1
	v_and_b32_e32 v0, 32, v0
	v_bitop3_b32 v2, v1, s0, v0 bitop3:0xde
	s_lshl_b32 s0, s3, 5
	s_and_b32 s79, s0, 0x60
	s_lshl_b32 s0, s79, 7
	s_waitcnt vmcnt(6)
	s_ashr_i32 s96, s78, 31
	s_add_i32 s21, s74, 0xc000
	v_bitop3_b32 v0, v1, s0, v0 bitop3:0xde
	s_cmp_lt_u32 s3, 4
	v_mov_b32_e32 v9, v8
	v_mov_b32_e32 v10, v8
	v_mov_b32_e32 v11, v8
	s_cselect_b64 s[68:69], -1, 0
	s_add_i32 s75, s74, 0xe000
	s_ashr_i32 s66, s8, 31
	s_mov_b32 s67, 0
	v_add_u32_e32 v164, 0, v0
	v_add_u32_e32 v165, 0, v2
	s_mov_b64 s[42:43], s[54:55]
	s_mov_b64 s[0:1], s[54:55]
	s_barrier
	s_branch .LBB0_1416

.LBB0_1493:
	s_add_u32 s8, s0, 0x58000000
	s_addc_u32 s9, s1, 0
	s_add_i32 s75, s62, 0x18000
	s_mov_b32 m0, s75
	s_movk_i32 s13, 0x80
	s_add_i32 s76, s62, 0x1a000
	buffer_load_dwordx4 v199, s[52:55], s13 offen lds
	s_mov_b32 m0, s76
	s_add_i32 s77, s62, 0x8000
	buffer_load_dwordx4 v228, s[52:55], s13 offen lds
	s_mov_b32 s42, s54
	s_mov_b32 s43, s55
	s_mov_b32 m0, s77
	s_add_i32 s80, s62, 0xa000
	buffer_load_dwordx4 v229, s[40:43], s13 offen lds
	s_mov_b32 m0, s80
	s_add_i32 s82, s62, 0x1c000
	buffer_load_dwordx4 v252, s[40:43], s13 offen lds
	s_mov_b32 m0, s82
	s_mov_b32 s13, 0x40080
	s_add_i32 s83, s62, 0x1e000
	buffer_load_dwordx4 v199, s[52:55], s13 offen lds
	s_mov_b32 m0, s83
	s_sext_i32_i8 s78, s4
	buffer_load_dwordx4 v228, s[52:55], s13 offen lds
	s_waitcnt vmcnt(8)
	s_barrier
	s_and_b32 s4, s5, 3
	v_and_b32_e32 v1, 48, v0
	v_lshlrev_b32_e32 v2, 6, v0
	s_movk_i32 s13, 0x3c0
	v_lshlrev_b32_e32 v0, 2, v0
	s_lshl_b32 s88, s12, 6
	s_lshl_b32 s12, s12, 13
	v_and_or_b32 v1, v2, s13, v1
	v_and_b32_e32 v0, 32, v0
	s_lshl_b32 s89, s4, 5
	s_lshl_b32 s4, s4, 12
	s_waitcnt vmcnt(6)
	s_add_i32 s90, s62, 0xc000
	v_bitop3_b32 v2, v1, s12, v0 bitop3:0xde
	v_bitop3_b32 v0, v1, s4, v0 bitop3:0xde
	s_cmp_lt_u32 s5, 4
	v_mov_b32_e32 v9, v8
	v_mov_b32_e32 v10, v8
	v_mov_b32_e32 v11, v8
	s_cselect_b64 s[18:19], -1, 0
	s_ashr_i32 s91, s88, 31
	s_add_i32 s92, s62, 0xe000
	s_ashr_i32 s93, s33, 31
	s_mov_b32 s94, 0
	v_add_u32_e32 v176, 0, v0
	v_add_u32_e32 v198, 0, v2
	s_mov_b64 s[42:43], s[54:55]
	s_mov_b64 s[4:5], s[54:55]
	s_barrier
	s_branch .LBB0_1496

.LBB0_1525:
	s_add_u32 s0, s0, 0x800000
	s_addc_u32 s1, s1, 0
	s_add_i32 s75, s59, 0x18000
	s_mov_b32 m0, s75
	s_movk_i32 s5, 0x80
	s_add_i32 s76, s59, 0x1a000
	buffer_load_dwordx4 v170, s[52:55], s5 offen lds
	s_mov_b32 m0, s76
	s_add_i32 s77, s59, 0x8000
	buffer_load_dwordx4 v171, s[52:55], s5 offen lds
	s_mov_b32 s42, s54
	s_mov_b32 s43, s55
	s_mov_b32 m0, s77
	s_add_i32 s82, s59, 0xa000
	buffer_load_dwordx4 v172, s[40:43], s5 offen lds
	s_mov_b32 m0, s82
	s_add_i32 s83, s59, 0x1c000
	buffer_load_dwordx4 v173, s[40:43], s5 offen lds
	s_mov_b32 m0, s83
	s_mov_b32 s5, 0x80080
	s_add_i32 s88, s59, 0x1e000
	buffer_load_dwordx4 v170, s[52:55], s5 offen lds
	s_mov_b32 m0, s88
	v_and_b32_e32 v1, 48, v0
	buffer_load_dwordx4 v171, s[52:55], s5 offen lds
	s_waitcnt vmcnt(8)
	s_barrier
	v_lshlrev_b32_e32 v2, 6, v0
	s_movk_i32 s5, 0x3c0
	v_lshlrev_b32_e32 v0, 2, v0
	s_and_b32 s89, s8, 3
	s_lshl_b32 s90, s4, 6
	s_lshl_b32 s4, s4, 13
	v_and_or_b32 v1, v2, s5, v1
	v_and_b32_e32 v0, 32, v0
	v_bitop3_b32 v2, v1, s4, v0 bitop3:0xde
	s_lshl_b32 s91, s89, 5
	s_lshl_b32 s4, s89, 12
	s_waitcnt vmcnt(6)
	s_add_i32 s92, s59, 0xc000
	v_bitop3_b32 v0, v1, s4, v0 bitop3:0xde
	s_cmp_lt_u32 s8, 4
	v_mov_b32_e32 v49, v48
	v_mov_b32_e32 v50, v48
	v_mov_b32_e32 v51, v48
	s_cselect_b64 s[8:9], -1, 0
	s_ashr_i32 s93, s90, 31
	s_add_i32 s94, s59, 0xe000
	s_ashr_i32 s95, s33, 31
	s_ashr_i32 s96, s64, 31
	s_mov_b32 s78, 0
	v_add_u32_e32 v174, 0, v0
	v_add_u32_e32 v175, 0, v2
	s_mov_b64 s[42:43], s[54:55]
	s_mov_b64 s[4:5], s[54:55]
	s_barrier
	s_branch .LBB0_1528

.LBB0_1709:
	s_add_u32 s8, s18, 0x380000
	v_and_b32_e32 v5, 48, v4
	v_lshlrev_b32_e32 v6, 6, v4
	s_movk_i32 s5, 0x3c0
	v_lshlrev_b32_e32 v4, 2, v4
	s_addc_u32 s9, s19, 0
	s_and_b32 s3, s4, 3
	s_lshl_b32 s82, s2, 6
	s_lshl_b32 s2, s2, 13
	v_and_or_b32 v5, v6, s5, v5
	v_and_b32_e32 v4, 32, v4
	v_bitop3_b32 v6, v5, s2, v4 bitop3:0xde
	s_lshl_b32 s2, s3, 12
	s_add_u32 s18, s18, 0x31000000
	s_addc_u32 s19, s19, 0
	s_add_i32 s83, s70, 0x18000
	v_bitop3_b32 v7, v5, s2, v4 bitop3:0xde
	s_mov_b32 s42, s54
	s_mov_b32 s43, s55
	s_mov_b32 m0, s83
	s_movk_i32 s2, 0x80
	s_add_i32 s88, s70, 0x1a000
	buffer_load_dwordx4 v136, s[40:43], s2 offen lds
	s_mov_b32 m0, s88
	s_add_i32 s89, s70, 0x8000
	buffer_load_dwordx4 v137, s[40:43], s2 offen lds
	v_mbcnt_lo_u32_b32 v4, -1, 0
	v_mbcnt_hi_u32_b32 v4, -1, v4
	s_mov_b32 m0, s89
	v_lshl_add_u32 v4, v4, 4, s71
	ds_read_b64 v[4:5], v4
	s_add_i32 s90, s70, 0xa000
	s_add_i32 s91, s70, 0x1c000
	s_add_i32 s92, s70, 0x1e000
	s_add_i32 s93, s70, 0xc000
	s_waitcnt lgkmcnt(0)
	buffer_load_dwordx4 v4, s[52:55], s2 offen lds
	s_mov_b32 m0, s90
	s_cmp_lt_u32 s4, 4
	buffer_load_dwordx4 v5, s[52:55], s2 offen lds
	s_mov_b32 m0, s91
	s_mov_b32 s2, 0x40080
	buffer_load_dwordx4 v136, s[40:43], s2 offen lds
	s_mov_b32 m0, s92
	v_mov_b32_e32 v1, v0
	buffer_load_dwordx4 v137, s[40:43], s2 offen lds
	s_waitcnt vmcnt(8)
	s_barrier
	s_waitcnt vmcnt(6)
	v_mov_b32_e32 v2, v0
	v_mov_b32_e32 v3, v0
	s_cselect_b64 s[22:23], -1, 0
	s_lshl_b32 s94, s3, 4
	s_add_i32 s95, s70, 0x24000
	s_add_i32 s96, s70, 0xe000
	s_mov_b32 s3, 0
	v_add_u32_e32 v138, 0, v7
	v_add_u32_e32 v139, 0, v6
	s_mov_b64 s[44:45], s[52:53]
	s_mov_b64 s[46:47], s[54:55]
	s_mov_b64 s[66:67], s[54:55]
	s_barrier
	s_branch .LBB0_1712

.LBB0_1815:
	s_add_u32 s2, s2, 0x48600000
	s_addc_u32 s3, s3, 0
	s_add_i32 s69, s61, 0x18000
	s_mov_b32 m0, s69
	s_movk_i32 s8, 0x80
	s_add_i32 s70, s61, 0x1a000
	buffer_load_dwordx4 v130, s[52:55], s8 offen lds
	s_mov_b32 m0, s70
	s_add_i32 s71, s61, 0x8000
	buffer_load_dwordx4 v131, s[52:55], s8 offen lds
	s_mov_b32 s42, s54
	s_mov_b32 s43, s55
	s_mov_b32 m0, s71
	s_add_i32 s72, s61, 0xa000
	buffer_load_dwordx4 v132, s[40:43], s8 offen lds
	s_mov_b32 m0, s72
	s_add_i32 s73, s61, 0x1c000
	buffer_load_dwordx4 v133, s[40:43], s8 offen lds
	s_mov_b32 m0, s73
	s_mov_b32 s8, 0xb0080
	s_add_i32 s74, s61, 0x1e000
	buffer_load_dwordx4 v130, s[52:55], s8 offen lds
	s_mov_b32 m0, s74
	v_and_b32_e32 v5, 48, v4
	buffer_load_dwordx4 v131, s[52:55], s8 offen lds
	s_waitcnt vmcnt(8)
	s_barrier
	v_lshlrev_b32_e32 v6, 6, v4
	s_movk_i32 s8, 0x3c0
	v_lshlrev_b32_e32 v4, 2, v4
	s_lshl_b32 s75, s5, 6
	s_lshl_b32 s5, s5, 13
	v_and_or_b32 v5, v6, s8, v5
	v_and_b32_e32 v4, 32, v4
	v_bitop3_b32 v6, v5, s5, v4 bitop3:0xde
	s_lshl_b32 s5, s4, 5
	s_and_b32 s76, s5, 0x60
	s_lshl_b32 s5, s76, 7
	s_waitcnt vmcnt(6)
	s_add_i32 s77, s61, 0xc000
	v_bitop3_b32 v4, v5, s5, v4 bitop3:0xde
	s_cmp_lt_u32 s4, 4
	v_mov_b32_e32 v1, v0
	v_mov_b32_e32 v2, v0
	v_mov_b32_e32 v3, v0
	s_cselect_b64 s[8:9], -1, 0
	s_ashr_i32 s78, s75, 31
	s_add_i32 s79, s61, 0xe000
	s_ashr_i32 s80, s33, 31
	s_mov_b32 s82, 0
	v_add_u32_e32 v134, 0, v4
	v_add_u32_e32 v135, 0, v6
	s_mov_b64 s[42:43], s[54:55]
	s_mov_b64 s[4:5], s[54:55]
	s_barrier
	s_branch .LBB0_1818

.LBB0_1940:
	s_add_u32 s8, s4, 0x31000000
	s_addc_u32 s9, s5, 0
	s_add_u32 s18, s4, 0x800000
	s_addc_u32 s19, s5, 0
	s_add_i32 s76, s68, 0x18000
	s_mov_b32 m0, s76
	s_movk_i32 s1, 0x80
	s_add_i32 s77, s68, 0x1a000
	buffer_load_dwordx4 v134, s[52:55], s1 offen lds
	s_mov_b32 m0, s77
	s_add_i32 s78, s68, 0x8000
	buffer_load_dwordx4 v135, s[52:55], s1 offen lds
	s_mov_b32 s46, s54
	s_mov_b32 s47, s55
	s_mov_b32 m0, s78
	s_add_i32 s79, s68, 0xa000
	buffer_load_dwordx4 v136, s[44:47], s1 offen lds
	s_mov_b32 m0, s79
	s_add_i32 s80, s68, 0x1c000
	buffer_load_dwordx4 v137, s[44:47], s1 offen lds
	s_mov_b32 m0, s80
	s_mov_b32 s1, 0x80080
	s_add_i32 s82, s68, 0x1e000
	buffer_load_dwordx4 v134, s[52:55], s1 offen lds
	s_mov_b32 m0, s82
	v_and_b32_e32 v5, 48, v4
	buffer_load_dwordx4 v135, s[52:55], s1 offen lds
	s_waitcnt vmcnt(8)
	s_barrier
	s_sext_i32_i16 s1, s12
	v_lshlrev_b32_e32 v6, 6, v4
	s_movk_i32 s12, 0x3c0
	v_lshlrev_b32_e32 v4, 2, v4
	s_and_b32 s4, s13, 3
	s_lshl_b32 s5, s20, 13
	v_and_or_b32 v5, v6, s12, v5
	v_and_b32_e32 v4, 32, v4
	s_lshl_b32 s83, s20, 6
	v_bitop3_b32 v6, v5, s5, v4 bitop3:0xde
	s_lshl_b32 s5, s4, 12
	s_waitcnt vmcnt(6)
	s_add_i32 s88, s68, 0xc000
	v_bitop3_b32 v4, v5, s5, v4 bitop3:0xde
	s_cmp_lt_u32 s13, 4
	v_mov_b32_e32 v1, v0
	v_mov_b32_e32 v2, v0
	v_mov_b32_e32 v3, v0
	s_cselect_b64 s[20:21], -1, 0
	s_lshl_b32 s89, s4, 4
	s_add_i32 s90, s68, 0xe000
	s_ashr_i32 s91, s33, 31
	s_mov_b32 s92, 0
	s_mov_b64 s[4:5], -1
	v_add_u32_e32 v138, 0, v4
	v_add_u32_e32 v139, 0, v6
	s_mov_b64 s[46:47], s[54:55]
	s_mov_b64 s[12:13], s[54:55]
	s_barrier
	s_branch .LBB0_1943

.LBB0_2019:
	s_add_u32 s2, s4, 0x2d000000
	s_addc_u32 s3, s5, 0
	s_add_u32 s8, s4, 0x600000
	s_addc_u32 s9, s5, 0
	s_add_u32 s18, s4, 0x58000000
	s_addc_u32 s19, s5, 0
	s_add_i32 s72, s64, 0x18000
	s_mov_b32 m0, s72
	s_movk_i32 s4, 0x80
	s_add_i32 s73, s64, 0x1a000
	buffer_load_dwordx4 v174, s[52:55], s4 offen lds
	s_mov_b32 m0, s73
	s_add_i32 s74, s64, 0x8000
	buffer_load_dwordx4 v175, s[52:55], s4 offen lds
	s_mov_b32 s46, s54
	s_mov_b32 s47, s55
	s_mov_b32 m0, s74
	s_add_i32 s75, s64, 0xa000
	buffer_load_dwordx4 v176, s[44:47], s4 offen lds
	s_mov_b32 m0, s75
	s_add_i32 s76, s64, 0x1c000
	buffer_load_dwordx4 v198, s[44:47], s4 offen lds
	s_mov_b32 m0, s76
	s_mov_b32 s4, 0x164080
	s_add_i32 s77, s64, 0x1e000
	buffer_load_dwordx4 v174, s[52:55], s4 offen lds
	s_mov_b32 m0, s77
	v_and_b32_e32 v1, 48, v0
	buffer_load_dwordx4 v175, s[52:55], s4 offen lds
	s_waitcnt vmcnt(8)
	s_barrier
	v_lshlrev_b32_e32 v2, 6, v0
	s_movk_i32 s5, 0x3c0
	v_lshlrev_b32_e32 v0, 2, v0
	s_and_b32 s78, s12, 3
	s_lshl_b32 s4, s13, 13
	v_and_or_b32 v1, v2, s5, v1
	v_and_b32_e32 v0, 32, v0
	s_lshl_b32 s79, s13, 6
	v_bitop3_b32 v2, v1, s4, v0 bitop3:0xde
	s_lshl_b32 s82, s78, 5
	s_lshl_b32 s4, s78, 12
	s_waitcnt vmcnt(6)
	s_add_i32 s83, s64, 0xc000
	v_bitop3_b32 v0, v1, s4, v0 bitop3:0xde
	s_cmp_lt_u32 s12, 4
	v_mov_b32_e32 v49, v48
	v_mov_b32_e32 v50, v48
	v_mov_b32_e32 v51, v48
	s_cselect_b64 s[20:21], -1, 0
	s_ashr_i32 s88, s79, 31
	s_add_i32 s89, s64, 0xe000
	s_ashr_i32 s90, s33, 31
	s_ashr_i32 s91, s58, 31
	s_mov_b32 s92, 0
	v_add_u32_e32 v199, 0, v0
	v_add_u32_e32 v200, 0, v2
	s_mov_b64 s[46:47], s[54:55]
	s_mov_b64 s[4:5], s[54:55]
	s_barrier
	s_branch .LBB0_2022
